# E19: combine Wf LDS layout padded to 144-B lane stride (bank-conflict-free ds_read_b128) on top of E13
# speedup vs baseline: 1.0067x; 1.0048x over previous
.LBB0_1838:
	s_andn2_b64 vcc, exec, s[0:1]
	s_cbranch_vccnz .LBB0_1924
	v_readlane_b32 s0, v253, 21
	s_add_i32 s24, s54, 1
	s_cmp_eq_u32 s54, 3
	v_mov_b32_e32 v1, s0
	s_waitcnt vmcnt(0)
	ds_read_b64 v[2:3], v1
	s_cselect_b64 s[2:3], -1, 0
	s_cmp_lg_u32 s54, 3
	v_readfirstlane_b32 s0, v0
	s_cselect_b64 s[8:9], -1, 0
	s_waitcnt lgkmcnt(0)
	v_readfirstlane_b32 s7, v3
	v_readfirstlane_b32 s6, v2
	s_and_b64 vcc, exec, s[2:3]
	s_cbranch_vccnz .LBB0_1841
	v_readlane_b32 s1, v253, 51
	v_mov_b32_e32 v5, v101
	v_add_u32_e32 v12, 0x400, v0
	v_mov_b32_e32 v1, s1
	ds_read_b64 v[2:3], v1
	s_mul_i32 s1, s24, 0xb08000
	v_lshlrev_b32_e32 v1, 4, v0
	v_and_b32_e32 v4, 16, v1
	v_add_u32_e32 v14, 0x600, v0
	s_waitcnt lgkmcnt(0)
	v_readfirstlane_b32 s4, v2
	v_readfirstlane_b32 s5, v3
	s_add_u32 s4, s4, s1
	s_addc_u32 s5, s5, 0
	v_lshl_add_u64 v[2:3], s[4:5], 0, v[4:5]
	s_mov_b64 s[4:5], 0x2c00
	v_add_u32_e32 v4, 0x200, v0
	v_lshl_add_u64 v[10:11], v[2:3], 0, s[4:5]
	v_ashrrev_i32_e32 v2, 1, v0
	s_movk_i32 s1, 0x2c20
	v_ashrrev_i32_e32 v4, 1, v4
	v_ashrrev_i32_e32 v12, 1, v12
	v_ashrrev_i32_e32 v14, 1, v14
	v_mad_i64_i32 v[2:3], s[4:5], v2, s1, v[10:11]
	v_mad_i64_i32 v[6:7], s[4:5], v4, s1, v[10:11]
	v_mad_i64_i32 v[12:13], s[4:5], v12, s1, v[10:11]
	v_mad_i64_i32 v[14:15], s[4:5], v14, s1, v[10:11]
	global_load_dwordx4 v[2:5], v[2:3], off
	s_nop 0
	global_load_dwordx4 v[6:9], v[6:7], off
	s_nop 0
	global_load_dwordx4 v[10:13], v[12:13], off
	s_nop 0
	global_load_dwordx4 v[14:17], v[14:15], off
	v_lshrrev_b32_e32 v18, 3, v0
	v_add_lshl_u32 v1, v0, v18, 4
	s_waitcnt vmcnt(3)
	ds_write_b128 v1, v[2:5]
	s_waitcnt vmcnt(2)
	ds_write_b128 v1, v[6:9] offset:9216
	s_waitcnt vmcnt(1)
	ds_write_b128 v1, v[10:13] offset:18432
	s_waitcnt vmcnt(0)
	ds_write_b128 v1, v[14:17] offset:27648

.LBB0_1848:
	v_lshlrev_b32_e32 v14, 4, v1
	s_nop 1
	global_load_dwordx4 v[2:5], v14, s[12:13]
	global_load_dwordx4 v[6:9], v14, s[12:13] offset:1024
	global_load_dwordx4 v[10:13], v14, s[12:13] offset:2048
	s_nop 0
	global_load_dwordx4 v[14:17], v14, s[12:13] offset:3072
	s_add_u32 s16, s6, 0x100000
	s_addc_u32 s25, s7, 0
	s_lshl_b32 s26, s54, 2
	s_lshl_b32 s4, s24, 2
	s_and_b64 s[2:3], exec, s[2:3]
	s_cselect_b32 s27, 0, s4
	s_ashr_i32 s11, s10, 31
	s_lshl_b64 s[4:5], s[10:11], 11
	v_or_b32_e32 v74, s4, v18
	v_mov_b32_e32 v75, s5
	s_lshl_b64 s[4:5], s[10:11], 12
	v_lshlrev_b32_e32 v66, 2, v1
	v_mul_u32_u24_e32 v19, 0x90, v1
	v_cmp_eq_u32_e64 s[2:3], 0, v1
	v_lshl_or_b32 v1, v1, 4, s4
	v_readlane_b32 s4, v253, 20
	s_add_i32 s4, s4, s18
	v_or_b32_e32 v68, 0x100, v66
	v_or_b32_e32 v70, 0x200, v66
	v_or_b32_e32 v72, 0x300, v66
	v_mov_b32_e32 v77, s5
	s_ashr_i32 s5, s4, 31
	v_add_u32_e32 v20, 0x2400, v19
	v_add_u32_e32 v21, 0x4800, v19
	v_add_u32_e32 v22, 0x6c00, v19
	s_lshl_b64 s[14:15], s[4:5], 13
	s_lshl_b64 s[4:5], s[4:5], 11
	v_mov_b32_e32 v62, v101
	v_mov_b32_e32 v63, v101
	v_or_b32_e32 v76, 0xc00, v1
	v_or_b32_e32 v78, s14, v18
	v_or_b32_e32 v80, s4, v18
	v_mov_b32_e32 v64, v101
	v_mov_b32_e32 v65, v101
	v_add_u32_e32 v1, 0, v19
	v_add_u32_e32 v67, 0, v20
	v_add_u32_e32 v69, 0, v21
	v_add_u32_e32 v71, 0, v22
	v_mov_b64_e32 v[58:59], v[62:63]
	v_mov_b64_e32 v[54:55], v[62:63]
	v_mov_b64_e32 v[50:51], v[62:63]
	v_mov_b64_e32 v[30:31], v[62:63]
	v_mov_b64_e32 v[38:39], v[62:63]
	v_mov_b64_e32 v[42:43], v[62:63]
	v_mov_b64_e32 v[46:47], v[62:63]
	v_mov_b64_e32 v[18:19], v[62:63]
	v_mov_b64_e32 v[22:23], v[62:63]
	v_mov_b64_e32 v[26:27], v[62:63]
	v_mov_b64_e32 v[34:35], v[62:63]
	s_lshl_b64 s[12:13], s[10:11], 5
	v_mov_b32_e32 v79, s15
	v_mov_b32_e32 v81, s5
	s_mov_b32 s11, -1
	v_mov_b64_e32 v[60:61], v[64:65]
	v_mov_b64_e32 v[56:57], v[64:65]
	v_mov_b64_e32 v[52:53], v[64:65]
	v_mov_b64_e32 v[32:33], v[64:65]
	v_mov_b64_e32 v[40:41], v[64:65]
	v_mov_b64_e32 v[44:45], v[64:65]
	v_mov_b64_e32 v[48:49], v[64:65]
	v_mov_b64_e32 v[20:21], v[64:65]
	v_mov_b64_e32 v[24:25], v[64:65]
	v_mov_b64_e32 v[28:29], v[64:65]
	v_mov_b64_e32 v[36:37], v[64:65]
	s_branch .LBB0_1850

.LBB0_1864:
	v_mul_f32_e32 v73, v124, v124
	v_mul_f32_e32 v100, v126, v126
	v_fmac_f32_e32 v73, v125, v125
	v_fmac_f32_e32 v100, v127, v127
	v_add_f32_e32 v73, v100, v73
	v_mul_f32_e32 v100, v128, v128
	v_mul_f32_e32 v140, v130, v130
	v_fmac_f32_e32 v100, v129, v129
	v_fmac_f32_e32 v140, v131, v131
	v_add_f32_e32 v100, v140, v100
	v_add_f32_e32 v73, v100, v73
	v_mul_f32_e32 v100, v132, v132
	v_mul_f32_e32 v140, v134, v134
	v_fmac_f32_e32 v100, v133, v133
	v_fmac_f32_e32 v140, v135, v135
	v_add_f32_e32 v100, v140, v100
	v_add_f32_e32 v73, v100, v73
	v_mul_f32_e32 v100, v136, v136
	v_mul_f32_e32 v140, v138, v138
	v_fmac_f32_e32 v100, v137, v137
	v_fmac_f32_e32 v140, v139, v139
	v_add_f32_e32 v100, v140, v100
	v_add_f32_e32 v73, v100, v73
	s_nop 1
	v_add_f32_dpp v73, v73, v73 quad_perm:[1,0,3,2] row_mask:0xf bank_mask:0xf bound_ctrl:1
	s_nop 1
	v_add_f32_dpp v73, v73, v73 quad_perm:[2,3,0,1] row_mask:0xf bank_mask:0xf bound_ctrl:1
	s_nop 1
	v_add_f32_dpp v73, v73, v73 row_half_mirror row_mask:0xf bank_mask:0xf bound_ctrl:1
	s_nop 1
	v_add_f32_dpp v73, v73, v73 row_mirror row_mask:0xf bank_mask:0xf bound_ctrl:1
	v_mov_b32_e32 v100, v73
	s_nop 1
	v_permlane16_swap_b32_e32 v73, v100
	v_add_f32_e32 v73, v73, v100
	v_mov_b32_e32 v100, v73
	s_nop 1
	v_permlane32_swap_b32_e32 v73, v100
	v_add_f32_e32 v73, v73, v100
	v_fmamk_f32 v73, v73, 0x3a800000, v215
	v_mul_f32_e32 v100, 0x4f800000, v73
	v_cmp_gt_f32_e32 vcc, s59, v73
	s_nop 1
	v_cndmask_b32_e32 v73, v73, v100, vcc
	v_sqrt_f32_e32 v100, v73
	s_nop 0
	v_add_u32_e32 v140, -1, v100
	v_fma_f32 v141, -v140, v100, v73
	v_cmp_ge_f32_e64 s[4:5], 0, v141
	v_add_u32_e32 v141, 1, v100
	s_nop 0
	v_cndmask_b32_e64 v140, v100, v140, s[4:5]
	v_fma_f32 v100, -v141, v100, v73
	v_cmp_lt_f32_e64 s[4:5], 0, v100
	s_nop 1
	v_cndmask_b32_e64 v100, v140, v141, s[4:5]
	v_mul_f32_e32 v140, 0x37800000, v100
	v_cndmask_b32_e32 v100, v100, v140, vcc
	v_cmp_class_f32_e32 vcc, v73, v212
	s_nop 1
	v_cndmask_b32_e32 v73, v100, v73, vcc
	v_div_scale_f32 v100, s[4:5], v73, v73, 1.0
	v_rcp_f32_e32 v140, v100
	s_mov_b64 s[4:5], -1
	v_fma_f32 v141, -v100, v140, 1.0
	v_fmac_f32_e32 v140, v141, v140
	v_div_scale_f32 v141, vcc, 1.0, v73, 1.0
	v_mul_f32_e32 v144, v141, v140
	v_fma_f32 v145, -v100, v144, v141
	v_fmac_f32_e32 v144, v145, v140
	v_fma_f32 v100, -v100, v144, v141
	v_div_fmas_f32 v100, v100, v140, v144
	v_div_fixup_f32 v140, v100, v73, 1.0
	v_mov_b32_e32 v141, v140
	s_and_b64 vcc, exec, s[0:1]
	s_cbranch_vccnz .LBB0_1868
	v_mov_b32_e32 v144, v140
	v_mov_b32_e32 v145, v140
	v_pk_mul_f32 v[146:147], v[126:127], v[144:145]
	v_pk_mul_f32 v[148:149], v[124:125], v[140:141]
	v_pk_fma_f32 v[162:163], v[48:49], v[146:147], v[36:37]
	v_pk_fma_f32 v[164:165], v[46:47], v[148:149], v[34:35]
	ds_read_b128 v[146:149], v1
	s_mov_b32 s4, 0x37000000
	v_add_co_u32_e32 v142, vcc, s4, v142
	v_cvt_pk_bf16_f32 v150, v164, v165
	v_cvt_pk_bf16_f32 v151, v162, v163
	v_addc_co_u32_e32 v143, vcc, 0, v143, vcc
	global_store_dwordx2 v[142:143], v[150:151], off
	ds_read_b128 v[150:153], v1 offset:16
	ds_read_b128 v[154:157], v1 offset:32
	ds_read_b128 v[158:161], v1 offset:48
	s_waitcnt lgkmcnt(3)
	v_fma_f32 v73, v164, v146, 0
	v_fma_f32 v100, v164, v147, 0
	v_fma_f32 v166, v164, v148, 0
	v_fma_f32 v167, v164, v149, 0
	ds_read_b128 v[146:149], v1 offset:64
	s_waitcnt lgkmcnt(3)
	v_fma_f32 v168, v164, v150, 0
	v_fma_f32 v169, v164, v151, 0
	v_fma_f32 v170, v164, v152, 0
	v_fma_f32 v171, v164, v153, 0
	ds_read_b128 v[150:153], v1 offset:80
	s_waitcnt lgkmcnt(3)
	v_fmac_f32_e32 v73, v165, v154
	v_fmac_f32_e32 v100, v165, v155
	v_fmac_f32_e32 v166, v165, v156
	v_fmac_f32_e32 v167, v165, v157
	s_waitcnt lgkmcnt(1)
	v_fmac_f32_e32 v73, v162, v146
	v_fmac_f32_e32 v100, v162, v147
	v_fmac_f32_e32 v166, v162, v148
	v_fmac_f32_e32 v167, v162, v149
	ds_read_b128 v[146:149], v1 offset:96
	v_fmac_f32_e32 v168, v165, v158
	v_fmac_f32_e32 v169, v165, v159
	v_fmac_f32_e32 v170, v165, v160
	v_fmac_f32_e32 v171, v165, v161
	s_waitcnt lgkmcnt(1)
	v_fmac_f32_e32 v168, v162, v150
	v_fmac_f32_e32 v169, v162, v151
	v_fmac_f32_e32 v170, v162, v152
	v_fmac_f32_e32 v171, v162, v153
	ds_read_b128 v[150:153], v1 offset:112
	s_waitcnt lgkmcnt(1)
	v_fmac_f32_e32 v73, v163, v146
	v_fmac_f32_e32 v100, v163, v147
	v_fmac_f32_e32 v166, v163, v148
	v_fmac_f32_e32 v167, v163, v149
	v_pk_mul_f32 v[146:147], v[130:131], v[144:145]
	v_pk_mul_f32 v[148:149], v[128:129], v[140:141]
	v_pk_fma_f32 v[154:155], v[44:45], v[146:147], v[28:29]
	v_pk_fma_f32 v[156:157], v[42:43], v[148:149], v[26:27]
	ds_read_b128 v[146:149], v67
	s_waitcnt lgkmcnt(1)
	v_fmac_f32_e32 v168, v163, v150
	v_fmac_f32_e32 v169, v163, v151
	v_cvt_pk_bf16_f32 v150, v156, v157
	v_cvt_pk_bf16_f32 v151, v154, v155
	v_fmac_f32_e32 v170, v163, v152
	v_fmac_f32_e32 v171, v163, v153
	global_store_dwordx2 v[142:143], v[150:151], off offset:512
	ds_read_b128 v[150:153], v67 offset:16
	s_waitcnt lgkmcnt(1)
	v_fmac_f32_e32 v73, v156, v146
	v_fmac_f32_e32 v100, v156, v147
	v_fmac_f32_e32 v166, v156, v148
	v_fmac_f32_e32 v167, v156, v149
	ds_read_b128 v[146:149], v1 offset:9248
	s_waitcnt lgkmcnt(1)
	v_fmac_f32_e32 v168, v156, v150
	v_fmac_f32_e32 v169, v156, v151
	v_fmac_f32_e32 v170, v156, v152
	v_fmac_f32_e32 v171, v156, v153
	ds_read_b128 v[150:153], v1 offset:9264
	s_waitcnt lgkmcnt(1)
	v_fmac_f32_e32 v73, v157, v146
	v_fmac_f32_e32 v100, v157, v147
	v_fmac_f32_e32 v166, v157, v148
	v_fmac_f32_e32 v167, v157, v149
	ds_read_b128 v[146:149], v1 offset:9280
	s_waitcnt lgkmcnt(1)
	v_fmac_f32_e32 v168, v157, v150
	v_fmac_f32_e32 v169, v157, v151
	v_fmac_f32_e32 v170, v157, v152
	v_fmac_f32_e32 v171, v157, v153
	ds_read_b128 v[150:153], v1 offset:9296
	s_waitcnt lgkmcnt(1)
	v_fmac_f32_e32 v73, v154, v146
	v_fmac_f32_e32 v100, v154, v147
	v_fmac_f32_e32 v166, v154, v148
	v_fmac_f32_e32 v167, v154, v149
	ds_read_b128 v[146:149], v1 offset:9312
	s_waitcnt lgkmcnt(1)
	v_fmac_f32_e32 v168, v154, v150
	v_fmac_f32_e32 v169, v154, v151
	v_fmac_f32_e32 v170, v154, v152
	v_fmac_f32_e32 v171, v154, v153
	ds_read_b128 v[150:153], v1 offset:9328
	s_waitcnt lgkmcnt(1)
	v_fmac_f32_e32 v73, v155, v146
	v_fmac_f32_e32 v100, v155, v147
	v_fmac_f32_e32 v166, v155, v148
	v_fmac_f32_e32 v167, v155, v149
	v_pk_mul_f32 v[146:147], v[134:135], v[144:145]
	v_pk_mul_f32 v[148:149], v[132:133], v[140:141]
	v_pk_fma_f32 v[162:163], v[40:41], v[146:147], v[24:25]
	v_pk_fma_f32 v[164:165], v[38:39], v[148:149], v[22:23]
	ds_read_b128 v[146:149], v69
	s_waitcnt lgkmcnt(1)
	v_fmac_f32_e32 v168, v155, v150
	v_fmac_f32_e32 v169, v155, v151
	v_cvt_pk_bf16_f32 v150, v164, v165
	v_cvt_pk_bf16_f32 v151, v162, v163
	v_fmac_f32_e32 v170, v155, v152
	v_fmac_f32_e32 v171, v155, v153
	global_store_dwordx2 v[142:143], v[150:151], off offset:1024
	ds_read_b128 v[150:153], v69 offset:16
	s_waitcnt lgkmcnt(1)
	v_fmac_f32_e32 v73, v164, v146
	v_fmac_f32_e32 v100, v164, v147
	v_fmac_f32_e32 v166, v164, v148
	v_fmac_f32_e32 v167, v164, v149
	ds_read_b128 v[146:149], v1 offset:18464
	s_waitcnt lgkmcnt(1)
	v_fmac_f32_e32 v168, v164, v150
	v_fmac_f32_e32 v169, v164, v151
	v_fmac_f32_e32 v170, v164, v152
	v_fmac_f32_e32 v171, v164, v153
	ds_read_b128 v[150:153], v1 offset:18480
	ds_read_b128 v[154:157], v1 offset:18496
	ds_read_b128 v[158:161], v1 offset:18512
	s_waitcnt lgkmcnt(3)
	v_fmac_f32_e32 v73, v165, v146
	v_fmac_f32_e32 v100, v165, v147
	v_fmac_f32_e32 v166, v165, v148
	v_fmac_f32_e32 v167, v165, v149
	ds_read_b128 v[146:149], v1 offset:18528
	s_waitcnt lgkmcnt(3)
	v_fmac_f32_e32 v168, v165, v150
	v_fmac_f32_e32 v169, v165, v151
	v_fmac_f32_e32 v170, v165, v152
	v_fmac_f32_e32 v171, v165, v153
	ds_read_b128 v[150:153], v1 offset:18544
	s_waitcnt lgkmcnt(3)
	v_fmac_f32_e32 v73, v162, v154
	v_fmac_f32_e32 v100, v162, v155
	s_waitcnt lgkmcnt(2)
	v_fmac_f32_e32 v170, v162, v160
	v_fmac_f32_e32 v171, v162, v161
	s_waitcnt lgkmcnt(1)
	v_fmac_f32_e32 v73, v163, v146
	v_fmac_f32_e32 v100, v163, v147
	v_pk_mul_f32 v[144:145], v[138:139], v[144:145]
	v_pk_mul_f32 v[146:147], v[136:137], v[140:141]
	s_waitcnt lgkmcnt(0)
	v_fmac_f32_e32 v170, v163, v152
	v_fmac_f32_e32 v171, v163, v153
	v_pk_fma_f32 v[152:153], v[32:33], v[144:145], v[20:21]
	v_pk_fma_f32 v[154:155], v[30:31], v[146:147], v[18:19]
	ds_read_b128 v[144:147], v71
	v_fmac_f32_e32 v166, v162, v156
	v_fmac_f32_e32 v167, v162, v157
	v_fmac_f32_e32 v168, v162, v158
	v_fmac_f32_e32 v169, v162, v159
	v_fmac_f32_e32 v166, v163, v148
	v_fmac_f32_e32 v167, v163, v149
	v_cvt_pk_bf16_f32 v148, v154, v155
	v_cvt_pk_bf16_f32 v149, v152, v153
	v_fmac_f32_e32 v168, v163, v150
	v_fmac_f32_e32 v169, v163, v151
	global_store_dwordx2 v[142:143], v[148:149], off offset:1536
	ds_read_b128 v[148:151], v71 offset:16
	s_waitcnt lgkmcnt(1)
	v_fmac_f32_e32 v73, v154, v144
	v_fmac_f32_e32 v100, v154, v145
	ds_read_b128 v[142:145], v1 offset:27680
	v_fmac_f32_e32 v166, v154, v146
	v_fmac_f32_e32 v167, v154, v147
	s_waitcnt lgkmcnt(1)
	v_fmac_f32_e32 v168, v154, v148
	v_fmac_f32_e32 v169, v154, v149
	ds_read_b128 v[146:149], v1 offset:27696
	s_waitcnt lgkmcnt(1)
	v_fmac_f32_e32 v73, v155, v142
	v_fmac_f32_e32 v100, v155, v143
	v_fmac_f32_e32 v166, v155, v144
	v_fmac_f32_e32 v167, v155, v145
	ds_read_b128 v[142:145], v1 offset:27712
	v_fmac_f32_e32 v170, v154, v150
	v_fmac_f32_e32 v171, v154, v151
	s_waitcnt lgkmcnt(1)
	v_fmac_f32_e32 v168, v155, v146
	v_fmac_f32_e32 v169, v155, v147
	v_fmac_f32_e32 v170, v155, v148
	v_fmac_f32_e32 v171, v155, v149
	ds_read_b128 v[146:149], v1 offset:27728
	s_waitcnt lgkmcnt(1)
	v_fmac_f32_e32 v73, v152, v142
	v_fmac_f32_e32 v100, v152, v143
	v_fmac_f32_e32 v166, v152, v144
	v_fmac_f32_e32 v167, v152, v145
	ds_read_b128 v[142:145], v1 offset:27744
	s_waitcnt lgkmcnt(1)
	v_fmac_f32_e32 v168, v152, v146
	v_fmac_f32_e32 v169, v152, v147
	v_fmac_f32_e32 v170, v152, v148
	v_fmac_f32_e32 v171, v152, v149
	ds_read_b128 v[146:149], v1 offset:27760
	s_waitcnt lgkmcnt(1)
	v_fmac_f32_e32 v73, v153, v142
	v_fmac_f32_e32 v100, v153, v143
	v_fmac_f32_e32 v166, v153, v144
	v_add_f32_dpp v73, v73, v73 quad_perm:[1,0,3,2] row_mask:0xf bank_mask:0xf bound_ctrl:1
	v_fmac_f32_e32 v167, v153, v145
	s_waitcnt lgkmcnt(0)
	v_fmac_f32_e32 v168, v153, v146
	v_add_f32_dpp v73, v73, v73 quad_perm:[2,3,0,1] row_mask:0xf bank_mask:0xf bound_ctrl:1
	v_fmac_f32_e32 v169, v153, v147
	v_fmac_f32_e32 v170, v153, v148
	v_add_f32_dpp v73, v73, v73 row_half_mirror row_mask:0xf bank_mask:0xf bound_ctrl:1
	v_fmac_f32_e32 v171, v153, v149
	s_nop 0
	v_add_f32_dpp v73, v73, v73 row_mirror row_mask:0xf bank_mask:0xf bound_ctrl:1
	v_mov_b32_e32 v142, v73
	s_nop 1
	v_permlane16_swap_b32_e32 v73, v142
	v_add_f32_e32 v142, v73, v142
	s_nop 0
	v_add_f32_dpp v73, v100, v100 quad_perm:[1,0,3,2] row_mask:0xf bank_mask:0xf bound_ctrl:1
	v_mov_b32_e32 v144, v142
	s_nop 1
	v_permlane32_swap_b32_e32 v142, v144
	v_add_f32_dpp v73, v73, v73 quad_perm:[2,3,0,1] row_mask:0xf bank_mask:0xf bound_ctrl:1
	s_nop 1
	v_add_f32_dpp v73, v73, v73 row_half_mirror row_mask:0xf bank_mask:0xf bound_ctrl:1
	s_nop 1
	v_add_f32_dpp v73, v73, v73 row_mirror row_mask:0xf bank_mask:0xf bound_ctrl:1
	v_mov_b32_e32 v100, v73
	s_nop 1
	v_permlane16_swap_b32_e32 v73, v100
	v_add_f32_e32 v143, v73, v100
	s_nop 0
	v_add_f32_dpp v73, v166, v166 quad_perm:[1,0,3,2] row_mask:0xf bank_mask:0xf bound_ctrl:1
	v_mov_b32_e32 v145, v143
	s_nop 1
	v_permlane32_swap_b32_e32 v143, v145
	v_add_f32_dpp v73, v73, v73 quad_perm:[2,3,0,1] row_mask:0xf bank_mask:0xf bound_ctrl:1
	s_nop 1
	v_add_f32_dpp v73, v73, v73 row_half_mirror row_mask:0xf bank_mask:0xf bound_ctrl:1
	s_nop 1
	v_add_f32_dpp v73, v73, v73 row_mirror row_mask:0xf bank_mask:0xf bound_ctrl:1
	v_mov_b32_e32 v100, v73
	s_nop 1
	v_permlane16_swap_b32_e32 v73, v100
	v_add_f32_e32 v146, v73, v100
	s_nop 0
	v_add_f32_dpp v73, v167, v167 quad_perm:[1,0,3,2] row_mask:0xf bank_mask:0xf bound_ctrl:1
	v_mov_b32_e32 v148, v146
	s_nop 1
	v_permlane32_swap_b32_e32 v146, v148
	v_add_f32_dpp v73, v73, v73 quad_perm:[2,3,0,1] row_mask:0xf bank_mask:0xf bound_ctrl:1
	s_nop 1
	v_add_f32_dpp v73, v73, v73 row_half_mirror row_mask:0xf bank_mask:0xf bound_ctrl:1
	s_nop 1
	v_add_f32_dpp v73, v73, v73 row_mirror row_mask:0xf bank_mask:0xf bound_ctrl:1
	v_mov_b32_e32 v100, v73
	s_nop 1
	v_permlane16_swap_b32_e32 v73, v100
	v_add_f32_e32 v147, v73, v100
	s_nop 0
	v_add_f32_dpp v73, v168, v168 quad_perm:[1,0,3,2] row_mask:0xf bank_mask:0xf bound_ctrl:1
	v_mov_b32_e32 v149, v147
	s_nop 1
	v_permlane32_swap_b32_e32 v147, v149
	v_add_f32_dpp v73, v73, v73 quad_perm:[2,3,0,1] row_mask:0xf bank_mask:0xf bound_ctrl:1
	s_nop 1
	v_add_f32_dpp v73, v73, v73 row_half_mirror row_mask:0xf bank_mask:0xf bound_ctrl:1
	s_nop 1
	v_add_f32_dpp v73, v73, v73 row_mirror row_mask:0xf bank_mask:0xf bound_ctrl:1
	v_mov_b32_e32 v100, v73
	s_nop 1
	v_permlane16_swap_b32_e32 v73, v100
	v_add_f32_e32 v150, v73, v100
	s_nop 0
	v_add_f32_dpp v73, v169, v169 quad_perm:[1,0,3,2] row_mask:0xf bank_mask:0xf bound_ctrl:1
	v_mov_b32_e32 v152, v150
	s_nop 1
	v_permlane32_swap_b32_e32 v150, v152
	v_add_f32_dpp v73, v73, v73 quad_perm:[2,3,0,1] row_mask:0xf bank_mask:0xf bound_ctrl:1
	s_nop 1
	v_add_f32_dpp v73, v73, v73 row_half_mirror row_mask:0xf bank_mask:0xf bound_ctrl:1
	s_nop 1
	v_add_f32_dpp v73, v73, v73 row_mirror row_mask:0xf bank_mask:0xf bound_ctrl:1
	v_mov_b32_e32 v100, v73
	s_nop 1
	v_permlane16_swap_b32_e32 v73, v100
	v_add_f32_e32 v151, v73, v100
	s_nop 0
	v_add_f32_dpp v73, v170, v170 quad_perm:[1,0,3,2] row_mask:0xf bank_mask:0xf bound_ctrl:1
	v_mov_b32_e32 v153, v151
	s_nop 1
	v_permlane32_swap_b32_e32 v151, v153
	v_add_f32_dpp v73, v73, v73 quad_perm:[2,3,0,1] row_mask:0xf bank_mask:0xf bound_ctrl:1
	s_nop 1
	v_add_f32_dpp v73, v73, v73 row_half_mirror row_mask:0xf bank_mask:0xf bound_ctrl:1
	s_nop 1
	v_add_f32_dpp v73, v73, v73 row_mirror row_mask:0xf bank_mask:0xf bound_ctrl:1
	v_mov_b32_e32 v100, v73
	s_nop 1
	v_permlane16_swap_b32_e32 v73, v100
	v_add_f32_e32 v154, v73, v100
	s_nop 0
	v_add_f32_dpp v73, v171, v171 quad_perm:[1,0,3,2] row_mask:0xf bank_mask:0xf bound_ctrl:1
	v_mov_b32_e32 v156, v154
	s_nop 1
	v_permlane32_swap_b32_e32 v154, v156
	v_add_f32_dpp v73, v73, v73 quad_perm:[2,3,0,1] row_mask:0xf bank_mask:0xf bound_ctrl:1
	s_nop 1
	v_add_f32_dpp v73, v73, v73 row_half_mirror row_mask:0xf bank_mask:0xf bound_ctrl:1
	s_nop 1
	v_add_f32_dpp v73, v73, v73 row_mirror row_mask:0xf bank_mask:0xf bound_ctrl:1
	v_mov_b32_e32 v100, v73
	s_nop 1
	v_permlane16_swap_b32_e32 v73, v100
	v_add_f32_e32 v155, v73, v100
	v_mov_b32_e32 v157, v155
	s_nop 1
	v_permlane32_swap_b32_e32 v155, v157
	s_and_saveexec_b64 s[4:5], s[2:3]
	s_cbranch_execz .LBB0_1867
	s_add_u32 s18, s6, s12
	v_pk_add_f32 v[146:147], v[146:147], v[148:149]
	v_pk_add_f32 v[144:145], v[142:143], v[144:145]
	s_addc_u32 s19, s7, s13
	v_pk_add_f32 v[154:155], v[154:155], v[156:157]
	v_pk_add_f32 v[152:153], v[150:151], v[152:153]
	global_store_dwordx4 v213, v[144:147], s[18:19]
	global_store_dwordx4 v213, v[152:155], s[18:19] offset:16
